# early L1 invalidate (wave 1) also on the first grid barrier
# baseline (speedup 1.0000x reference)
; __device__ __forceinline__ unsigned xb_ld(unsigned* p)              { return __hip_atomic_load(p, __ATOMIC_RELAXED, __HIP_MEMORY_SCOPE_AGENT); }
; __device__ __forceinline__ unsigned xb_add(unsigned* p, unsigned v) { return __hip_atomic_fetch_add(p, v, __ATOMIC_RELAXED, __HIP_MEMORY_SCOPE_AGENT); }
; __device__ __forceinline__ void xcd_barrier_complete(unsigned* bar, unsigned x, unsigned& nloc, unsigned& nx) {
;     const unsigned G = gridDim.x * gridDim.y * gridDim.z;
;     unsigned sum, cnt, mine, sp = 0u;
;     for (;;) {
;         sum = 0u; cnt = 0u; mine = 0u;
; #pragma unroll
;         for (unsigned j = 0; j < 16; ++j) { const unsigned c = xb_ld(&bar[XB_XCNT(j)]); sum += c; cnt += (c > 0u) ? 1u : 0u; mine = (j == x) ? c : mine; }
;         if (sum == G) break;
;         __builtin_amdgcn_s_sleep(1);
;         if ((++sp & 255u) == 0u) { if (xb_ld(&bar[XB_TMO])) break; if (sp > XB_SPIN_CAP) { atomicAdd(&bar[XB_TMO], 1u); break; } }
;     }
;     nloc = mine > 0u ? mine : 1u; nx = cnt > 0u ? cnt : 1u;
; }
; __device__ __forceinline__ void xcd_barrier(const XcdBarrier& b) {
;     asm volatile("s_waitcnt vmcnt(0)" ::: "memory");
;     __syncthreads();
;     if (threadIdx.x == 0) {
;         unsigned* bar = b.bar;
;         __builtin_amdgcn_s_waitcnt(0);
;         unsigned nloc = b.st[0], nx = b.st[1];
;         if (nloc == 0u) { xcd_barrier_complete(bar, b.x, nloc, nx); b.st[0] = nloc; b.st[1] = nx; }
;         const unsigned old = xb_add(&bar[XB_XSUB(b.x)], 1u);
;         const unsigned gen = old / nloc;
;         if (old + 1u == (gen + 1u) * nloc) {
;             __builtin_amdgcn_fence(__ATOMIC_RELEASE, "agent");
;             asm volatile("s_waitcnt vmcnt(0)" ::: "memory");
;             const unsigned og = xb_add(&bar[XB_TOP], 1u);
;             const unsigned tg = og / nx;
;             if (og + 1u == (tg + 1u) * nx) xb_add(&bar[XB_TOPGEN], 1u);
;             else XB_SPIN(xb_ld(&bar[XB_TOPGEN]) == tg, bar);
;             __builtin_amdgcn_fence(__ATOMIC_ACQUIRE, "agent");
;             xb_add(&bar[XB_XGEN(b.x)], 1u);
;             asm volatile("s_waitcnt vmcnt(0)" ::: "memory");
;         } else {
;             XB_SPIN(xb_ld(&bar[XB_XGEN(b.x)]) == gen, bar);
;             __builtin_amdgcn_fence(__ATOMIC_ACQUIRE, "agent");
;             asm volatile("s_waitcnt vmcnt(0)" ::: "memory");
;         }
;     }
;     __syncthreads();
.LBB0_36:
	s_or_b64 exec, exec, s[0:1]
	s_cmp_lt_i32 s95, 2
	s_cbranch_scc1 .LBB0_87
	s_waitcnt vmcnt(0)
	v_cmp_eq_u32_e32 vcc, 0, v0
	s_barrier
	v_readfirstlane_b32 s2, v0
	s_nop 3
	s_lshr_b32 s2, s2, 6
	s_cmp_lg_u32 s2, 1
	s_cbranch_scc1 .Lgbf_noinv
	buffer_inv sc1
.Lgbf_noinv:
	s_and_saveexec_b64 s[0:1], vcc
	s_cbranch_execz .LBB0_86
	v_readlane_b32 s2, v246, 22
	s_waitcnt vmcnt(0) expcnt(0) lgkmcnt(0)
	s_nop 0
	v_mov_b32_e32 v1, s2
	ds_read_b32 v3, v1
	ds_read_b32 v1, v1 offset:4
	s_waitcnt lgkmcnt(1)
	v_cmp_ne_u32_e32 vcc, 0, v3
	s_cbranch_vccnz .LBB0_54
	v_readlane_b32 s4, v246, 0
	v_readlane_b32 s5, v246, 1
	s_load_dwordx2 s[2:3], s[4:5], 0x4
	s_add_u32 s4, s92, 0x4200
	s_addc_u32 s5, s93, 0
	s_add_u32 s6, s92, 0x4400
	s_addc_u32 s7, s93, 0
	s_waitcnt lgkmcnt(0)
	s_mul_i32 s33, s2, s97
	s_add_u32 s2, s92, 0x4500
	s_mul_i32 s33, s33, s3
	s_addc_u32 s3, s93, 0
	s_add_u32 s8, s92, 0x4600
	s_addc_u32 s9, s93, 0
	s_add_u32 s10, s92, 0x4700
	s_addc_u32 s11, s93, 0
	s_add_u32 s12, s92, 0x4800
	s_addc_u32 s13, s93, 0
	s_add_u32 s14, s92, 0x4900
	s_addc_u32 s15, s93, 0
	s_add_u32 s16, s92, 0x4a00
	s_addc_u32 s17, s93, 0
	s_add_u32 s18, s92, 0x4b00
	s_addc_u32 s19, s93, 0
	s_add_u32 s20, s92, 0x4c00
	s_addc_u32 s21, s93, 0
	s_add_u32 s22, s92, 0x4d00
	s_addc_u32 s23, s93, 0
	s_add_u32 s24, s92, 0x4e00
	s_addc_u32 s25, s93, 0
	s_add_u32 s26, s92, 0x4f00
	s_addc_u32 s27, s93, 0
	s_add_u32 s28, s92, 0x5000
	s_addc_u32 s29, s93, 0
	s_add_u32 s30, s92, 0x5100
	s_addc_u32 s31, s93, 0
	s_add_u32 s34, s92, 0x5200
	s_addc_u32 s35, s93, 0
	s_add_u32 s58, s92, 0x5300
	s_addc_u32 s59, s93, 0
	s_mov_b32 s36, 1
	v_mov_b32_e32 v17, 0
	s_branch .LBB0_41

; __device__ __forceinline__ unsigned xb_ld(unsigned* p)              { return __hip_atomic_load(p, __ATOMIC_RELAXED, __HIP_MEMORY_SCOPE_AGENT); }
; __device__ __forceinline__ unsigned xb_add(unsigned* p, unsigned v) { return __hip_atomic_fetch_add(p, v, __ATOMIC_RELAXED, __HIP_MEMORY_SCOPE_AGENT); }
; #define XB_SPIN(cond, bar) do { unsigned _sp = 0; while (cond) { __builtin_amdgcn_s_sleep(1); \
;     if ((++_sp & 255u) == 0u) { if (xb_ld(&(bar)[XB_TMO])) break; if (_sp > XB_SPIN_CAP) { atomicAdd(&(bar)[XB_TMO], 1u); break; } } } } while (0)
; __device__ __forceinline__ void xcd_barrier(const XcdBarrier& b) {
;     ...
;             else XB_SPIN(xb_ld(&bar[XB_TOPGEN]) == tg, bar);
;             __builtin_amdgcn_fence(__ATOMIC_ACQUIRE, "agent");
;             xb_add(&bar[XB_XGEN(b.x)], 1u);
;             asm volatile("s_waitcnt vmcnt(0)" ::: "memory");
;         } else {
;             XB_SPIN(xb_ld(&bar[XB_XGEN(b.x)]) == gen, bar);
;             __builtin_amdgcn_fence(__ATOMIC_ACQUIRE, "agent");
;             asm volatile("s_waitcnt vmcnt(0)" ::: "memory");
.LBB0_67:
	s_or_b64 exec, exec, s[6:7]
	s_waitcnt vmcnt(0)
	s_nop 0
	s_waitcnt vmcnt(0)

; __device__ __forceinline__ unsigned xb_ld(unsigned* p)              { return __hip_atomic_load(p, __ATOMIC_RELAXED, __HIP_MEMORY_SCOPE_AGENT); }
; __device__ __forceinline__ unsigned xb_add(unsigned* p, unsigned v) { return __hip_atomic_fetch_add(p, v, __ATOMIC_RELAXED, __HIP_MEMORY_SCOPE_AGENT); }
; #define XB_SPIN(cond, bar) do { unsigned _sp = 0; while (cond) { __builtin_amdgcn_s_sleep(1); \
;     if ((++_sp & 255u) == 0u) { if (xb_ld(&(bar)[XB_TMO])) break; if (_sp > XB_SPIN_CAP) { atomicAdd(&(bar)[XB_TMO], 1u); break; } } } } while (0)
; __device__ __forceinline__ void xcd_barrier(const XcdBarrier& b) {
;     ...
;             __builtin_amdgcn_fence(__ATOMIC_RELEASE, "agent");
;             asm volatile("s_waitcnt vmcnt(0)" ::: "memory");
;             const unsigned og = xb_add(&bar[XB_TOP], 1u);
;             const unsigned tg = og / nx;
;             if (og + 1u == (tg + 1u) * nx) xb_add(&bar[XB_TOPGEN], 1u);
;             else XB_SPIN(xb_ld(&bar[XB_TOPGEN]) == tg, bar);
;             __builtin_amdgcn_fence(__ATOMIC_ACQUIRE, "agent");
;             xb_add(&bar[XB_XGEN(b.x)], 1u);
;             asm volatile("s_waitcnt vmcnt(0)" ::: "memory");
;         } else {
;             XB_SPIN(xb_ld(&bar[XB_XGEN(b.x)]) == gen, bar);
;             __builtin_amdgcn_fence(__ATOMIC_ACQUIRE, "agent");
;             asm volatile("s_waitcnt vmcnt(0)" ::: "memory");
;         }
;     }
;     __syncthreads();
; __device__ __forceinline__ void phase1(const Args& a, int lane, int wave, int vcu, int G) {
;     const float* mod = (const float*)(a.ws + WS_MOD); bf16* H = (bf16*)(a.ws + RA_H); const float* g = a.in[6];
;     for (int m = vcu * 8 + wave; m < MROWS; m += G * 8) {
;         const float* xr = m < NT ? a.in[0] + (size_t)m * 2048 : a.in[2] + (size_t)(m - NT) * 2048;
;         const float* mr = mod + (size_t)(m < NT ? (m >> 11) : 8) * 12288;
;         f32x4 v[8]; float ss = 0.f;
; #pragma unroll
;         for (int j = 0; j < 8; ++j) { v[j] = __builtin_nontemporal_load((const f32x4*)(xr + 4 * (lane + 64 * j))); ss += v[j][0] * v[j][0] + v[j][1] * v[j][1] + v[j][2] * v[j][2] + v[j][3] * v[j][3]; }
.LBB0_85:
	s_or_b64 exec, exec, s[2:3]
	v_mov_b32_e32 v1, 0x2000
	v_mov_b32_e32 v2, 1
	s_waitcnt vmcnt(0)
	s_nop 0
	global_atomic_add v1, v2, s[4:5] offset:1024
	s_waitcnt vmcnt(0)
.LBB0_86:
	s_or_b64 exec, exec, s[0:1]
	s_waitcnt vmcnt(0)
	s_waitcnt lgkmcnt(0)
	s_barrier
.LBB0_87:
	s_cmp_gt_i32 s94, 1
	s_cselect_b64 s[0:1], -1, 0
	s_cmp_lt_i32 s95, 2
	s_cselect_b64 s[2:3], -1, 0
	s_or_b64 s[0:1], s[0:1], s[2:3]
	s_and_b64 vcc, exec, s[0:1]
	s_cbranch_vccnz .LBB0_143
	v_mov_b32_e32 v1, v0
	s_nop 0
	v_readfirstlane_b32 s0, v1
	s_ashr_i32 s1, s0, 6
	v_readlane_b32 s0, v246, 2
	s_lshl_b32 s2, s0, 3
	s_add_i32 s0, s1, s2
	s_cmpk_gt_i32 s0, 0x47ff
	s_cbranch_scc1 .LBB0_93
	v_lshlrev_b32_e32 v1, 2, v1
	v_and_b32_e32 v2, 0xfc, v1
	v_mov_b32_e32 v5, 0
	v_lshlrev_b32_e32 v4, 2, v2
	v_or_b32_e32 v12, 0x400, v2
	s_waitcnt lgkmcnt(0)
	v_lshl_add_u64 v[26:27], s[80:81], 0, v[4:5]
	v_or_b32_e32 v14, 0x500, v2
	v_lshlrev_b32_e32 v4, 2, v12
	v_or_b32_e32 v16, 0x600, v2
	v_lshl_add_u64 v[28:29], s[80:81], 0, v[4:5]
	v_lshlrev_b32_e32 v4, 2, v14
	v_or_b32_e32 v18, 0x700, v2
	v_lshl_add_u64 v[30:31], s[80:81], 0, v[4:5]
	v_lshlrev_b32_e32 v4, 2, v16
	v_lshl_add_u64 v[32:33], s[80:81], 0, v[4:5]
	v_lshlrev_b32_e32 v4, 2, v18
	v_lshl_add_u64 v[34:35], s[80:81], 0, v[4:5]
	v_lshlrev_b32_e32 v4, 1, v2
	s_add_u32 s16, s92, 0x100000
	v_lshl_add_u64 v[4:5], s[92:93], 0, v[4:5]
	s_mov_b64 s[4:5], 0x1a200000
	s_addc_u32 s17, s93, 0
	s_lshl_b32 s0, s97, 3
	v_lshl_add_u64 v[36:37], v[4:5], 0, s[4:5]
	s_ashr_i32 s3, s1, 31
	s_ashr_i32 s5, s2, 31
	s_add_u32 s4, s1, s2
	s_addc_u32 s5, s3, s5
	s_ashr_i32 s1, s0, 31
	s_lshl_b64 s[2:3], s[4:5], 13
	v_or_b32_e32 v6, 0x100, v2
	v_or_b32_e32 v8, 0x200, v2
	v_or_b32_e32 v10, 0x300, v2
	s_add_u32 s6, s68, s2
	s_addc_u32 s7, s69, s3
	s_lshl_b64 s[8:9], s[0:1], 13
	s_mov_b32 s11, 0
	v_lshlrev_b32_e32 v1, 2, v2
	v_lshlrev_b32_e32 v41, 2, v12
	v_lshlrev_b32_e32 v42, 2, v14
	v_lshlrev_b32_e32 v43, 2, v16
	v_lshlrev_b32_e32 v44, 2, v18
	v_mov_b32_e32 v45, 0x358637bd
	v_mov_b32_e32 v46, 0x3a000000
	s_mov_b32 s18, 0x800000
	s_movk_i32 s19, 0x7fff
	s_mov_b32 s20, 0xffff0000
	v_lshlrev_b32_e32 v47, 2, v6
	v_lshlrev_b32_e32 v48, 2, v8
	v_lshlrev_b32_e32 v49, 2, v10
	global_load_dwordx4 v[90:93], v[26:27], off
	global_load_dwordx4 v[94:97], v[26:27], off offset:1024
	global_load_dwordx4 v[98:101], v[26:27], off offset:2048
	global_load_dwordx4 v[102:105], v[26:27], off offset:3072
	global_load_dwordx4 v[106:109], v[28:29], off
	global_load_dwordx4 v[110:113], v[30:31], off
	global_load_dwordx4 v[114:117], v[32:33], off
	global_load_dwordx4 v[118:121], v[34:35], off
	s_cmpk_lt_i32 s4, 0x4000
	s_mov_b64 s[12:13], s[6:7]
	s_cbranch_scc1 .Lp1_lat_a
	s_add_i32 s26, s4, 0xffffc000
	s_mov_b32 s27, 0
	s_lshl_b64 s[26:27], s[26:27], 13
	s_add_u32 s12, s72, s26
	s_addc_u32 s13, s73, s27
